# adaLN partial sums handed to the hcat phase through a flag counter (write-through stores + per-block publish); first grid barrier is arrive-only and awaited before the second; hcat issues its row load
# speedup vs baseline: 1.0208x; 1.0142x over previous
.LBB0_7:
	s_or_b64 exec, exec, s[22:23]
	s_waitcnt vmcnt(0)
	s_barrier
	v_readfirstlane_b32 s100, v186
	s_nop 0
	s_cmp_lg_u32 s100, 0
	s_cbranch_scc1 .Lada_pub_skip
	v_readlane_b32 s100, v235, 7
	v_readlane_b32 s101, v235, 8
	v_mov_b32_e32 v236, 0x80
	v_mov_b32_e32 v237, 1
	s_mov_b64 exec, 1
	s_nop 1
	global_atomic_add v236, v237, s[100:101]
	s_mov_b64 exec, -1
.Lada_pub_skip:
	s_load_dwordx4 s[24:27], s[46:47], 0x98
	s_waitcnt lgkmcnt(0)
	s_add_i32 s34, s34, s26
	s_cmpk_gt_i32 s34, 0xbf
	s_cbranch_scc1 .LBB0_22

.LBB0_12:
	ds_read2st64_b32 v[10:11], v7 offset1:8
	ds_read2st64_b32 v[12:13], v7 offset0:12 offset1:16
	ds_read2st64_b32 v[14:15], v7 offset0:20 offset1:24
	v_ashrrev_i32_e32 v8, 31, v4
	v_add_u32_e32 v37, 0x400, v5
	v_add_u32_e32 v38, 0x400, v4
	v_add_u32_e32 v9, 0x2000, v7
	v_ashrrev_i32_e32 v36, 31, v5
	v_add_u32_sdwa v39, v4, v8 dst_sel:DWORD dst_unused:UNUSED_PAD src0_sel:DWORD src1_sel:BYTE_3
	v_ashrrev_i32_e32 v40, 31, v38
	v_ashrrev_i32_e32 v41, 31, v37
	ds_read2st64_b32 v[16:17], v7 offset0:28 offset1:32
	ds_read2st64_b32 v[18:19], v7 offset0:36 offset1:40
	ds_read2st64_b32 v[20:21], v7 offset0:44 offset1:48
	ds_read2st64_b32 v[22:23], v7 offset0:52 offset1:56
	ds_read2st64_b32 v[24:25], v7 offset0:60 offset1:64
	ds_read2st64_b32 v[26:27], v7 offset0:68 offset1:72
	ds_read2st64_b32 v[28:29], v7 offset0:76 offset1:80
	ds_read2st64_b32 v[30:31], v7 offset0:84 offset1:88
	ds_read2st64_b32 v[32:33], v7 offset0:92 offset1:96
	ds_read2st64_b32 v[34:35], v7 offset0:100 offset1:108
	v_add_u32_e32 v6, -2, v6
	v_add_u32_sdwa v36, v5, v36 dst_sel:DWORD dst_unused:UNUSED_PAD src0_sel:DWORD src1_sel:BYTE_3
	v_mov_b32_e32 v7, v9
	v_ashrrev_i32_e32 v9, 8, v39
	v_add_u32_sdwa v38, v38, v40 dst_sel:DWORD dst_unused:UNUSED_PAD src0_sel:DWORD src1_sel:BYTE_3
	v_add_u32_sdwa v37, v37, v41 dst_sel:DWORD dst_unused:UNUSED_PAD src0_sel:DWORD src1_sel:BYTE_3
	s_add_i32 s36, s36, 4
	v_cmp_eq_u32_e64 s[0:1], 0, v6
	v_ashrrev_i32_e32 v36, 8, v36
	v_add_u32_e32 v9, s35, v9
	v_ashrrev_i32_e32 v40, 8, v38
	v_ashrrev_i32_e32 v41, 8, v37
	s_or_b64 s[28:29], s[0:1], s[28:29]
	v_add_u32_e32 v39, s35, v36
	v_mad_i64_i32 v[36:37], s[0:1], v9, s31, v[2:3]
	v_add_u32_e32 v9, s35, v41
	v_add_u32_e32 v60, s35, v40
	s_waitcnt lgkmcnt(12)
	v_pk_add_f32 v[10:11], v[10:11], 0 op_sel_hi:[1,0]
	s_waitcnt lgkmcnt(11)
	v_mov_b32_e32 v40, v12
	s_waitcnt lgkmcnt(10)
	v_mov_b32_e32 v41, v14
	v_mov_b32_e32 v14, v13
	v_mov_b32_e32 v42, v15
	s_waitcnt lgkmcnt(9)
	v_mov_b32_e32 v43, v17
	s_waitcnt lgkmcnt(8)
	v_mov_b32_e32 v17, v18
	v_pk_add_f32 v[10:11], v[10:11], v[40:41]
	v_pk_add_f32 v[14:15], v[14:15], 0 op_sel_hi:[1,0]
	v_mov_b32_e32 v44, v18
	s_waitcnt lgkmcnt(7)
	v_mov_b32_e32 v45, v20
	v_mov_b32_e32 v20, v19
	v_pk_add_f32 v[10:11], v[10:11], v[42:43]
	v_pk_add_f32 v[14:15], v[14:15], v[16:17]
	v_mov_b32_e32 v46, v21
	s_waitcnt lgkmcnt(6)
	v_mov_b32_e32 v47, v23
	s_waitcnt lgkmcnt(5)
	v_mov_b32_e32 v23, v24
	v_pk_add_f32 v[10:11], v[10:11], v[44:45]
	v_pk_add_f32 v[14:15], v[14:15], v[20:21]
	v_mov_b32_e32 v48, v24
	s_waitcnt lgkmcnt(4)
	v_mov_b32_e32 v49, v26
	v_mov_b32_e32 v26, v25
	v_pk_add_f32 v[10:11], v[10:11], v[46:47]
	v_pk_add_f32 v[14:15], v[14:15], v[22:23]
	v_mov_b32_e32 v56, v27
	s_waitcnt lgkmcnt(3)
	v_mov_b32_e32 v57, v29
	s_waitcnt lgkmcnt(2)
	v_mov_b32_e32 v29, v30
	v_pk_add_f32 v[10:11], v[10:11], v[48:49]
	v_pk_add_f32 v[14:15], v[14:15], v[26:27]
	v_mov_b32_e32 v58, v30
	s_waitcnt lgkmcnt(1)
	v_mov_b32_e32 v59, v32
	v_mov_b32_e32 v32, v31
	v_pk_add_f32 v[10:11], v[10:11], v[56:57]
	v_pk_add_f32 v[14:15], v[14:15], v[28:29]
	v_pk_add_f32 v[10:11], v[10:11], v[58:59]
	v_pk_add_f32 v[14:15], v[14:15], v[32:33]
	v_add_u32_e32 v5, 0x800, v5
	v_add_u32_e32 v4, 0x800, v4
	v_mov_b32_e32 v8, s36
	v_mad_i64_i32 v[38:39], s[0:1], v39, s31, v[2:3]
	v_mad_i64_i32 v[12:13], s[0:1], v60, s31, v[2:3]
	global_store_dword v[36:37], v10, off sc1
	global_store_dword v[38:39], v11, off sc1
	s_waitcnt lgkmcnt(0)
	v_pk_add_f32 v[10:11], v[14:15], v[34:35]
	v_mad_i64_i32 v[18:19], s[0:1], v9, s31, v[2:3]
	global_store_dword v[12:13], v10, off sc1
	global_store_dword v[18:19], v11, off sc1
	s_andn2_b64 exec, exec, s[28:29]
	s_cbranch_execnz .LBB0_12
	s_or_b64 exec, exec, s[28:29]
	v_lshlrev_b32_e32 v6, 9, v8
	s_or_b64 exec, exec, s[26:27]
	s_and_saveexec_b64 s[0:1], s[10:11]
	s_cbranch_execz .LBB0_16
	s_branch .LBB0_15

.LBB0_15:
	v_add_u32_e32 v6, v50, v6
	v_lshl_add_u32 v16, v6, 2, 0
	ds_read2st64_b32 v[6:7], v16 offset1:8
	ds_read2st64_b32 v[8:9], v16 offset0:12 offset1:20
	ds_read2st64_b32 v[10:11], v16 offset0:24 offset1:32
	ds_read2st64_b32 v[12:13], v16 offset0:36 offset1:44
	ds_read2st64_b32 v[14:15], v16 offset0:48 offset1:56
	s_waitcnt lgkmcnt(4)
	v_pk_add_f32 v[6:7], v[6:7], 0 op_sel_hi:[1,0]
	s_waitcnt lgkmcnt(3)
	v_pk_add_f32 v[6:7], v[6:7], v[8:9]
	s_waitcnt lgkmcnt(2)
	v_pk_add_f32 v[6:7], v[6:7], v[10:11]
	ds_read2st64_b32 v[8:9], v16 offset0:60 offset1:68
	ds_read2st64_b32 v[10:11], v16 offset0:72 offset1:80
	ds_read2st64_b32 v[16:17], v16 offset0:84 offset1:92
	s_waitcnt lgkmcnt(4)
	v_pk_add_f32 v[6:7], v[6:7], v[12:13]
	s_waitcnt lgkmcnt(3)
	v_pk_add_f32 v[6:7], v[6:7], v[14:15]
	s_waitcnt lgkmcnt(2)
	v_pk_add_f32 v[6:7], v[6:7], v[8:9]
	v_ashrrev_i32_e32 v8, 31, v4
	v_add_u32_sdwa v4, v4, v8 dst_sel:DWORD dst_unused:UNUSED_PAD src0_sel:DWORD src1_sel:BYTE_3
	v_ashrrev_i32_e32 v8, 31, v5
	v_ashrrev_i32_e32 v4, 8, v4
	v_add_u32_sdwa v5, v5, v8 dst_sel:DWORD dst_unused:UNUSED_PAD src0_sel:DWORD src1_sel:BYTE_3
	s_waitcnt lgkmcnt(1)
	v_pk_add_f32 v[6:7], v[6:7], v[10:11]
	v_ashrrev_i32_e32 v5, 8, v5
	v_add_u32_e32 v4, s35, v4
	s_waitcnt lgkmcnt(0)
	v_pk_add_f32 v[6:7], v[6:7], v[16:17]
	v_add_u32_e32 v8, s35, v5
	v_mad_i64_i32 v[4:5], s[26:27], v4, s31, v[2:3]
	v_mad_i64_i32 v[8:9], s[26:27], v8, s31, v[2:3]
	global_store_dword v[4:5], v6, off sc1
	global_store_dword v[8:9], v7, off sc1

.LBB0_21:
	ds_read2st64_b32 v[6:7], v5 offset1:12
	ds_read2st64_b32 v[8:9], v5 offset0:24 offset1:36
	ds_read2st64_b32 v[10:11], v5 offset0:48 offset1:60
	ds_read2st64_b32 v[12:13], v5 offset0:72 offset1:84
	v_ashrrev_i32_e32 v14, 31, v4
	s_waitcnt lgkmcnt(3)
	v_add_f32_e32 v6, 0, v6
	v_add_f32_e32 v6, v6, v7
	s_waitcnt lgkmcnt(2)
	v_add_f32_e32 v6, v6, v8
	v_add_f32_e32 v6, v6, v9
	v_add_u32_sdwa v14, v4, v14 dst_sel:DWORD dst_unused:UNUSED_PAD src0_sel:DWORD src1_sel:BYTE_3
	s_waitcnt lgkmcnt(1)
	v_add_f32_e32 v6, v6, v10
	v_ashrrev_i32_e32 v14, 8, v14
	v_add_f32_e32 v6, v6, v11
	v_add_u32_e32 v15, 0x200, v4
	v_cmp_lt_i32_e64 s[0:1], s30, v4
	v_add_u32_e32 v14, s35, v14
	s_waitcnt lgkmcnt(0)
	v_add_f32_e32 v6, v6, v12
	v_add_u32_e32 v5, 0x800, v5
	s_or_b64 s[24:25], s[0:1], s[24:25]
	v_mov_b32_e32 v4, v15
	v_mad_i64_i32 v[14:15], s[0:1], v14, s31, v[2:3]
	v_add_f32_e32 v6, v6, v13
	global_store_dword v[14:15], v6, off sc1
	s_andn2_b64 exec, exec, s[24:25]
	s_cbranch_execnz .LBB0_21
	s_branch .LBB0_7

.LBB0_84:
	s_waitcnt vmcnt(0)
	s_barrier
	s_mov_b32 s98, 0
	s_mov_b64 s[0:1], exec
	v_readlane_b32 s2, v235, 5
	v_readlane_b32 s3, v235, 6
	s_and_b64 s[2:3], s[0:1], s[2:3]
	v_writelane_b32 v235, s46, 14
	s_nop 1
	v_writelane_b32 v235, s47, 15
	s_mov_b64 exec, s[2:3]
	s_cbranch_execz .LBB0_137
	s_add_i32 s2, 0, 0x20000
	v_mov_b32_e32 v0, s2
	s_waitcnt vmcnt(0) expcnt(0) lgkmcnt(0)
	ds_read_b32 v2, v0
	s_add_i32 s2, 0, 0x20004
	v_mov_b32_e32 v0, s2
	ds_read_b32 v0, v0
	s_waitcnt lgkmcnt(1)
	v_cmp_ne_u32_e32 vcc, 0, v2
	s_cbranch_vccnz .LBB0_101
	s_load_dwordx4 s[40:43], s[46:47], 0x98
	s_load_dword s2, s[46:47], 0xa8
	s_mov_b32 s48, 1
	v_mov_b32_e32 v16, 0
	s_waitcnt lgkmcnt(0)
	s_mul_i32 s27, s43, s2
	s_add_u32 s2, s40, 0x1b6f200
	s_addc_u32 s3, s41, 0
	s_add_u32 s4, s40, 0x1b6f400
	s_addc_u32 s5, s41, 0
	s_add_u32 s6, s40, 0x1b6f500
	s_addc_u32 s7, s41, 0
	s_add_u32 s8, s40, 0x1b6f600
	s_addc_u32 s9, s41, 0
	s_add_u32 s10, s40, 0x1b6f700
	s_addc_u32 s11, s41, 0
	s_add_u32 s12, s40, 0x1b6f800
	s_addc_u32 s13, s41, 0
	s_add_u32 s14, s40, 0x1b6f900
	s_addc_u32 s15, s41, 0
	s_add_u32 s16, s40, 0x1b6fa00
	s_addc_u32 s17, s41, 0
	s_add_u32 s18, s40, 0x1b6fb00
	s_addc_u32 s19, s41, 0
	s_add_u32 s20, s40, 0x1b6fc00
	s_addc_u32 s21, s41, 0
	s_add_u32 s22, s40, 0x1b6fd00
	s_addc_u32 s23, s41, 0
	s_add_u32 s28, s40, 0x1b6fe00
	s_addc_u32 s29, s41, 0
	s_add_u32 s30, s40, 0x1b6ff00
	s_addc_u32 s31, s41, 0
	s_add_u32 s34, s40, 0x1b70000
	s_addc_u32 s35, s41, 0
	s_add_u32 s36, s40, 0x1b70100
	s_addc_u32 s37, s41, 0
	s_add_u32 s38, s40, 0x1b70200
	s_addc_u32 s39, s41, 0
	s_add_u32 s40, s40, 0x1b70300
	s_mul_i32 s27, s27, s42
	s_addc_u32 s41, s41, 0
	s_branch .LBB0_89

.Lxb_poll_0:
	v_readfirstlane_b32 s98, v236
	s_branch .Lxb_done_0

.LBB0_140:
	v_cndmask_b32_e64 v0, 0, 1, s[24:25]
	v_cmp_ne_u32_e64 s[6:7], 1, v0
	s_andn2_b64 vcc, exec, s[24:25]
	v_mbcnt_lo_u32_b32 v187, -1, 0
	s_cbranch_vccnz .LBB0_155
	s_waitcnt lgkmcnt(0)
	s_add_u32 s14, s0, 0x1adf000
	s_addc_u32 s15, s1, 0
	s_add_u32 s16, s0, 0x9f73000
	s_addc_u32 s17, s1, 0
	s_load_dwordx2 s[0:1], s[12:13], 0x0
	v_lshlrev_b32_e32 v183, 2, v148
	v_and_b32_e32 v1, 0xfc, v183
	v_mbcnt_hi_u32_b32 v2, -1, v187
	v_lshlrev_b32_e32 v150, 2, v1
	v_mov_b32_e32 v151, 0
	v_and_b32_e32 v3, 64, v2
	s_waitcnt lgkmcnt(0)
	v_lshl_add_u64 v[152:153], s[0:1], 0, v[150:151]
	s_movk_i32 s0, 0x1000
	v_add_u32_e32 v3, 64, v3
	v_xor_b32_e32 v4, 32, v2
	v_cmp_gt_i32_e32 vcc, s0, v148
	v_cmp_lt_i32_e64 s[0:1], v4, v3
	s_load_dwordx2 s[2:3], s[12:13], 0x10
	s_load_dwordx2 s[4:5], s[12:13], 0x30
	v_cndmask_b32_e64 v4, v2, v4, s[0:1]
	v_lshlrev_b32_e32 v189, 2, v4
	v_xor_b32_e32 v4, 16, v2
	v_cmp_lt_i32_e64 s[0:1], v4, v3
	v_ashrrev_i32_e32 v0, 6, v148
	v_lshlrev_b32_e32 v181, 3, v0
	v_cndmask_b32_e64 v4, v2, v4, s[0:1]
	v_lshlrev_b32_e32 v190, 2, v4
	v_xor_b32_e32 v4, 8, v2
	v_cmp_lt_i32_e64 s[0:1], v4, v3
	v_and_b32_e32 v188, 1, v0
	s_waitcnt lgkmcnt(0)
	v_lshl_add_u64 v[154:155], s[2:3], 0, v[150:151]
	v_cndmask_b32_e64 v4, v2, v4, s[0:1]
	v_lshlrev_b32_e32 v191, 2, v4
	v_xor_b32_e32 v4, 4, v2
	v_cmp_lt_i32_e64 s[0:1], v4, v3
	v_cmp_gt_i32_e64 s[8:9], 2, v0
	v_add_u32_e32 v195, 0x4000, v0
	v_cndmask_b32_e64 v4, v2, v4, s[0:1]
	v_lshlrev_b32_e32 v192, 2, v4
	v_xor_b32_e32 v4, 2, v2
	v_cmp_lt_i32_e64 s[0:1], v4, v3
	v_lshl_add_u64 v[156:157], s[4:5], 0, v[150:151]
	v_add_u32_e32 v196, 0, v150
	v_cndmask_b32_e64 v4, v2, v4, s[0:1]
	v_lshlrev_b32_e32 v193, 2, v4
	v_xor_b32_e32 v4, 1, v2
	v_cmp_lt_i32_e64 s[0:1], v4, v3
	v_lshlrev_b32_e32 v150, 1, v1
	v_or_b32_e32 v0, 0x100, v1
	v_cndmask_b32_e64 v2, v2, v4, s[0:1]
	v_lshlrev_b32_e32 v194, 2, v2
	v_or_b32_e32 v2, 0x200, v1
	v_or_b32_e32 v4, 0x300, v1
	v_max_i32_e32 v1, 0xe00, v148
	v_sub_u32_e32 v1, v1, v148
	v_add_u32_e32 v1, 0x1ff, v1
	v_lshrrev_b32_e32 v3, 9, v1
	v_add_u32_e32 v5, 1, v3
	s_movk_i32 s4, 0x7ff
	v_and_b32_e32 v6, 0x7ff, v3
	v_lshlrev_b16_e32 v3, 9, v3
	v_and_b32_e32 v3, 0x600, v3
	v_cmp_lt_u16_e64 s[2:3], 3, v6
	v_bitop3_b16 v6, v148, s4, v148 bitop3:0xc
	v_cmp_gt_u16_e64 s[4:5], v3, v6
	s_or_b64 s[2:3], s[4:5], s[2:3]
	s_xor_b64 s[4:5], s[2:3], -1
	s_mov_b32 s2, 0x100000
	s_movk_i32 s0, 0x1ff
	v_cmp_gt_u32_e64 s[2:3], s2, v1
	v_cmp_lt_u32_e64 s[0:1], s0, v1
	s_and_b64 s[2:3], s[4:5], s[2:3]
	v_and_b32_e32 v197, 0xfffffe, v5
	v_or_b32_e32 v185, 4, v181
	v_lshl_add_u64 v[158:159], s[16:17], 0, v[150:151]
	v_lshl_add_u32 v198, v197, 9, v148
	v_add_u32_e32 v149, 0x200, v148
	v_cmp_ne_u32_e64 s[10:11], v5, v197
	s_and_b64 s[18:19], s[0:1], s[2:3]
	v_add_u32_e32 v199, 0, v183
	s_movk_i32 s21, 0x800
	s_movk_i32 s23, 0x6000
	s_movk_i32 s27, 0xdff
	s_mov_b32 s20, 0x3a800000
	s_mov_b32 s22, 0x358637bd
	s_mov_b32 s36, 0x800000
	v_lshlrev_b32_e32 v160, 1, v0
	v_lshlrev_b32_e32 v162, 1, v2
	v_lshlrev_b32_e32 v164, 1, v4
	v_mov_b32_e32 v200, 0x358637bd
	s_mov_b32 s37, s52
	s_branch .LBB0_143

.LBB0_143:
	s_lshl_b32 s0, s37, 6
	v_add_u32_e32 v166, s0, v181
	v_ashrrev_i32_e32 v167, 31, v166
	v_lshlrev_b64 v[0:1], 12, v[166:167]
	v_or_b32_e32 v168, 1, v166
	v_lshl_add_u64 v[0:1], v[152:153], 0, v[0:1]
	v_ashrrev_i32_e32 v169, 31, v168
	global_load_dwordx4 v[128:131], v[0:1], off nt
	global_load_dwordx4 v[124:127], v[0:1], off offset:1024 nt
	global_load_dwordx4 v[96:99], v[0:1], off offset:2048 nt
	global_load_dwordx4 v[84:87], v[0:1], off offset:3072 nt
	v_lshlrev_b64 v[0:1], 12, v[168:169]
	v_or_b32_e32 v170, 2, v166
	v_lshl_add_u64 v[0:1], v[152:153], 0, v[0:1]
	v_ashrrev_i32_e32 v171, 31, v170
	global_load_dwordx4 v[132:135], v[0:1], off nt
	global_load_dwordx4 v[112:115], v[0:1], off offset:1024 nt
	global_load_dwordx4 v[100:103], v[0:1], off offset:2048 nt
	global_load_dwordx4 v[88:91], v[0:1], off offset:3072 nt
	v_lshlrev_b64 v[0:1], 12, v[170:171]
	v_or_b32_e32 v172, 3, v166
	v_lshl_add_u64 v[0:1], v[152:153], 0, v[0:1]
	v_ashrrev_i32_e32 v173, 31, v172
	global_load_dwordx4 v[136:139], v[0:1], off nt
	global_load_dwordx4 v[116:119], v[0:1], off offset:1024 nt
	global_load_dwordx4 v[104:107], v[0:1], off offset:2048 nt
	global_load_dwordx4 v[92:95], v[0:1], off offset:3072 nt
	v_lshlrev_b64 v[0:1], 12, v[172:173]
	v_lshl_add_u64 v[0:1], v[152:153], 0, v[0:1]
	global_load_dwordx4 v[140:143], v[0:1], off nt
	global_load_dwordx4 v[120:123], v[0:1], off offset:1024 nt
	global_load_dwordx4 v[108:111], v[0:1], off offset:2048 nt
	global_load_dwordx4 v[80:83], v[0:1], off offset:3072 nt
	v_add_u32_e32 v0, s0, v185
	v_ashrrev_i32_e32 v1, 31, v0
	v_lshlrev_b64 v[2:3], 12, v[0:1]
	v_or_b32_e32 v4, 1, v0
	v_or_b32_e32 v6, 2, v0
	v_or_b32_e32 v0, 3, v0
	s_lshl_b32 s38, s37, 1
	v_ashrrev_i32_e32 v5, 31, v4
	v_ashrrev_i32_e32 v7, 31, v6
	v_ashrrev_i32_e32 v1, 31, v0
	v_or_b32_e32 v8, s38, v188
	v_lshlrev_b64 v[4:5], 12, v[4:5]
	v_lshlrev_b64 v[6:7], 12, v[6:7]
	v_lshlrev_b64 v[0:1], 12, v[0:1]
	v_ashrrev_i32_e32 v9, 31, v8
	v_lshl_add_u64 v[2:3], v[152:153], 0, v[2:3]
	v_lshl_add_u64 v[4:5], v[152:153], 0, v[4:5]
	v_lshl_add_u64 v[6:7], v[152:153], 0, v[6:7]
	v_lshl_add_u64 v[0:1], v[152:153], 0, v[0:1]
	v_lshlrev_b64 v[8:9], 12, v[8:9]
	v_lshl_add_u64 v[144:145], v[154:155], 0, v[8:9]
	global_load_dwordx4 v[76:79], v[2:3], off nt
	global_load_dwordx4 v[60:63], v[2:3], off offset:1024 nt
	global_load_dwordx4 v[44:47], v[2:3], off offset:2048 nt
	global_load_dwordx4 v[20:23], v[2:3], off offset:3072 nt
	global_load_dwordx4 v[72:75], v[4:5], off nt
	global_load_dwordx4 v[56:59], v[4:5], off offset:1024 nt
	global_load_dwordx4 v[40:43], v[4:5], off offset:2048 nt
	global_load_dwordx4 v[24:27], v[4:5], off offset:3072 nt
	global_load_dwordx4 v[68:71], v[6:7], off nt
	global_load_dwordx4 v[52:55], v[6:7], off offset:1024 nt
	global_load_dwordx4 v[36:39], v[6:7], off offset:2048 nt
	global_load_dwordx4 v[28:31], v[6:7], off offset:3072 nt
	global_load_dwordx4 v[64:67], v[0:1], off nt
	global_load_dwordx4 v[48:51], v[0:1], off offset:1024 nt
	global_load_dwordx4 v[32:35], v[0:1], off offset:2048 nt
	global_load_dwordx4 v[16:19], v[0:1], off offset:3072 nt
	global_load_dwordx4 v[12:15], v[144:145], off
	global_load_dwordx4 v[8:11], v[144:145], off offset:1024
	global_load_dwordx4 v[4:7], v[144:145], off offset:2048
	s_nop 0
	global_load_dwordx4 v[0:3], v[144:145], off offset:3072
	s_waitcnt vmcnt(63) expcnt(7) lgkmcnt(15)
	v_readfirstlane_b32 s100, v186
	s_nop 0
	s_cmp_lg_u32 s100, 0
	s_cbranch_scc1 .Lada_wait_skip
	v_readlane_b32 s100, v235, 7
	v_readlane_b32 s101, v235, 8
	v_mov_b32_e32 v236, 0x80
	s_nop 3
.Lada_poll:
	global_load_dword v237, v236, s[100:101] sc1
	s_waitcnt vmcnt(0)
	v_readfirstlane_b32 s99, v237
	s_nop 0
	s_cmp_ge_u32 s99, 0xc0
	s_cbranch_scc1 .Lada_wait_skip
	s_sleep 1
	s_branch .Lada_poll
.Lada_wait_skip:
	s_barrier
	s_and_saveexec_b64 s[4:5], vcc
	s_cbranch_execz .LBB0_153
	s_load_dwordx2 s[28:29], s[12:13], 0x28
	s_ashr_i32 s39, s37, 7
	s_mov_b64 s[0:1], -1
	v_mov_b32_e32 v144, v148
	v_mov_b32_e32 v145, v183
	s_and_saveexec_b64 s[30:31], s[18:19]
	s_cbranch_execz .LBB0_150
	s_mov_b32 s40, s39
	s_mov_b64 s[34:35], 0
	v_mov_b32_e32 v146, v197
	v_mov_b32_e32 v147, v199
	v_mov_b64_e32 v[144:145], v[148:149]

.LBB0_155:
	v_writelane_b32 v238, s98, 0
	v_readlane_b32 s98, v235, 0
	v_readlane_b32 s99, v235, 1
	s_lshl_b32 s101, s26, 2
	v_add_u32_e32 v200, s33, v186
	v_mov_b32_e32 v201, s101
	s_load_dwordx2 s[100:101], s[46:47], 0x28
	v_mov_b32_e32 v207, 0x2aaaaaab
	v_lshlrev_b32_e32 v202, 2, v200
	v_cmp_gt_u32_e32 vcc, 0x12000, v202
	s_and_b64 exec, exec, vcc
	s_cbranch_execz .Lmodfin_end
	s_waitcnt lgkmcnt(0)
.Lmodfin_loop:
	v_lshrrev_b32_e32 v203, 2, v202
	v_mul_hi_u32 v204, v203, v207
	v_lshrrev_b32_e32 v204, 10, v204
	v_mul_u32_u24_e32 v204, 0x6000, v204
	v_sub_u32_e32 v204, v202, v204
	global_load_dword v208, v204, s[100:101]
	v_add_u32_e32 v205, 0x1adf000, v202
	global_load_dword v209, v205, s[98:99]
	v_add_u32_e32 v205, 0x12000, v205
	global_load_dword v210, v205, s[98:99]
	v_add_u32_e32 v205, 0x12000, v205
	global_load_dword v211, v205, s[98:99]
	v_add_u32_e32 v205, 0x12000, v205
	global_load_dword v212, v205, s[98:99]
	v_add_u32_e32 v205, 0x12000, v205
	global_load_dword v213, v205, s[98:99]
	v_add_u32_e32 v205, 0x12000, v205
	global_load_dword v214, v205, s[98:99]
	v_add_u32_e32 v205, 0x12000, v205
	global_load_dword v215, v205, s[98:99]
	v_add_u32_e32 v205, 0x12000, v205
	global_load_dword v216, v205, s[98:99]
	s_waitcnt vmcnt(0)
	v_add_f32_e32 v208, v208, v209
	v_add_f32_e32 v208, v208, v210
	v_add_f32_e32 v208, v208, v211
	v_add_f32_e32 v208, v208, v212
	v_add_f32_e32 v208, v208, v213
	v_add_f32_e32 v208, v208, v214
	v_add_f32_e32 v208, v208, v215
	v_add_f32_e32 v208, v208, v216
	global_store_dword v202, v208, s[98:99]
	v_add_u32_e32 v202, v202, v201
	v_cmp_gt_u32_e32 vcc, 0x12000, v202
	s_and_b64 exec, exec, vcc
	s_cbranch_execnz .Lmodfin_loop
.Lmodfin_end:
	s_mov_b64 exec, -1
	v_readlane_b32 s98, v238, 0
	s_waitcnt vmcnt(0)
	s_waitcnt lgkmcnt(0)
	s_barrier
	s_mov_b64 s[0:1], exec
	v_readlane_b32 s2, v235, 5
	v_readlane_b32 s3, v235, 6
	s_and_b64 s[2:3], s[0:1], s[2:3]
	s_xor_b64 s[0:1], s[2:3], s[0:1]
	s_mov_b64 exec, s[2:3]
	s_cbranch_execz .LBB0_208
	s_cmp_eq_u32 s98, 0
	s_cbranch_scc1 .Lxb_nopend_1
	v_readlane_b32 s100, v235, 7
	v_readlane_b32 s101, v235, 8
	v_mov_b32_e32 v237, 0x3400
	s_nop 3
.Lxb_pend_1:
	global_load_dword v238, v237, s[100:101] sc1
	s_waitcnt vmcnt(0)
	v_cmp_le_u32_e32 vcc, s98, v238
	s_cbranch_vccnz .Lxb_pendok_1
	s_sleep 1
	s_branch .Lxb_pend_1
.Lxb_pendok_1:
	s_mov_b32 s98, 0
.Lxb_nopend_1:
	s_add_i32 s2, 0, 0x20000
	v_mov_b32_e32 v0, s2
	s_waitcnt vmcnt(0) expcnt(0) lgkmcnt(0)
	ds_read_b32 v2, v0
	s_add_i32 s2, 0, 0x20004
	v_mov_b32_e32 v0, s2
	ds_read_b32 v0, v0
	s_waitcnt lgkmcnt(1)
	v_cmp_ne_u32_e32 vcc, 0, v2
	s_cbranch_vccnz .LBB0_171
	v_readlane_b32 s44, v235, 0
	v_readlane_b32 s47, v235, 3
	v_readlane_b32 s2, v235, 4
	v_readlane_b32 s45, v235, 1
	s_mul_i32 s27, s47, s2
	s_add_u32 s2, s44, 0x1b6f200
	s_addc_u32 s3, s45, 0
	s_add_u32 s4, s44, 0x1b6f400
	s_addc_u32 s5, s45, 0
	s_add_u32 s8, s44, 0x1b6f500
	s_addc_u32 s9, s45, 0
	s_add_u32 s10, s44, 0x1b6f600
	s_addc_u32 s11, s45, 0
	s_add_u32 s12, s44, 0x1b6f700
	s_addc_u32 s13, s45, 0
	s_add_u32 s14, s44, 0x1b6f800
	s_addc_u32 s15, s45, 0
	s_add_u32 s16, s44, 0x1b6f900
	s_addc_u32 s17, s45, 0
	s_add_u32 s18, s44, 0x1b6fa00
	s_addc_u32 s19, s45, 0
	s_add_u32 s20, s44, 0x1b6fb00
	s_addc_u32 s21, s45, 0
	s_add_u32 s22, s44, 0x1b6fc00
	s_addc_u32 s23, s45, 0
	s_add_u32 s28, s44, 0x1b6fd00
	s_addc_u32 s29, s45, 0
	s_add_u32 s30, s44, 0x1b6fe00
	s_addc_u32 s31, s45, 0
	s_add_u32 s34, s44, 0x1b6ff00
	s_addc_u32 s35, s45, 0
	s_add_u32 s36, s44, 0x1b70000
	s_addc_u32 s37, s45, 0
	s_add_u32 s38, s44, 0x1b70100
	s_addc_u32 s39, s45, 0
	s_add_u32 s40, s44, 0x1b70200
	s_addc_u32 s41, s45, 0
	v_readlane_b32 s46, v235, 2
	s_add_u32 s42, s44, 0x1b70300
	s_mul_i32 s27, s27, s46
	s_addc_u32 s43, s45, 0
	s_mov_b32 s50, 1
	v_mov_b32_e32 v16, 0
	s_branch .LBB0_159

.Lxb_poll_1:
	v_readlane_b32 s101, v235, 2
	s_nop 0
	s_mul_i32 s100, s101, 33
	s_lshr_b32 s100, s100, 6
	s_cmp_lt_u32 s101, 64
	s_cbranch_scc1 .Lxb_wait_1
	s_cmp_ge_u32 s52, s100
	s_cbranch_scc0 .Lxb_wait_1
	v_readfirstlane_b32 s98, v236
	s_branch .Lxb_done_1
.Lxb_wait_1:
	v_readlane_b32 s100, v235, 7
	v_readlane_b32 s101, v235, 8
	s_nop 4

.LBB0_293:
	s_waitcnt vmcnt(0)
	s_waitcnt vmcnt(0)
	s_barrier
	s_mov_b64 s[0:1], exec
	v_readlane_b32 s2, v235, 5
	v_readlane_b32 s3, v235, 6
	s_and_b64 s[2:3], s[0:1], s[2:3]
	s_xor_b64 s[0:1], s[2:3], s[0:1]
	s_mov_b64 exec, s[2:3]
	s_cbranch_execz .LBB0_346
	s_cmp_eq_u32 s98, 0
	s_cbranch_scc1 .Lxb_nopend_2
	v_readlane_b32 s100, v235, 7
	v_readlane_b32 s101, v235, 8
	v_mov_b32_e32 v237, 0x3400
	s_nop 3

.Lxb_nopend_2:
	s_add_i32 s2, 0, 0x20000
	v_mov_b32_e32 v0, s2
	s_waitcnt vmcnt(0) expcnt(0) lgkmcnt(0)
	ds_read_b32 v2, v0
	s_add_i32 s2, 0, 0x20004
	v_mov_b32_e32 v0, s2
	ds_read_b32 v0, v0
	s_waitcnt lgkmcnt(1)
	v_cmp_ne_u32_e32 vcc, 0, v2
	s_cbranch_vccnz .LBB0_309
	v_readlane_b32 s44, v235, 0
	v_readlane_b32 s47, v235, 3
	v_readlane_b32 s2, v235, 4
	v_readlane_b32 s45, v235, 1
	s_mul_i32 s27, s47, s2
	s_add_u32 s2, s44, 0x1b6f200
	s_addc_u32 s3, s45, 0
	s_add_u32 s8, s44, 0x1b6f400
	s_addc_u32 s9, s45, 0
	s_add_u32 s10, s44, 0x1b6f500
	s_addc_u32 s11, s45, 0
	s_add_u32 s12, s44, 0x1b6f600
	s_addc_u32 s13, s45, 0
	s_add_u32 s14, s44, 0x1b6f700
	s_addc_u32 s15, s45, 0
	s_add_u32 s16, s44, 0x1b6f800
	s_addc_u32 s17, s45, 0
	s_add_u32 s18, s44, 0x1b6f900
	s_addc_u32 s19, s45, 0
	s_add_u32 s20, s44, 0x1b6fa00
	s_addc_u32 s21, s45, 0
	s_add_u32 s22, s44, 0x1b6fb00
	s_addc_u32 s23, s45, 0
	s_add_u32 s28, s44, 0x1b6fc00
	s_addc_u32 s29, s45, 0
	s_add_u32 s30, s44, 0x1b6fd00
	s_addc_u32 s31, s45, 0
	s_add_u32 s34, s44, 0x1b6fe00
	s_addc_u32 s35, s45, 0
	s_add_u32 s36, s44, 0x1b6ff00
	s_addc_u32 s37, s45, 0
	s_add_u32 s38, s44, 0x1b70000
	s_addc_u32 s39, s45, 0
	s_add_u32 s40, s44, 0x1b70100
	s_addc_u32 s41, s45, 0
	s_add_u32 s42, s44, 0x1b70200
	s_addc_u32 s43, s45, 0
	v_readlane_b32 s46, v235, 2
	s_add_u32 s44, s44, 0x1b70300
	s_mul_i32 s27, s27, s46
	s_addc_u32 s45, s45, 0
	s_mov_b32 s53, 1
	v_mov_b32_e32 v16, 0
	s_branch .LBB0_297

.LBB0_373:
	s_waitcnt lgkmcnt(0)
	s_barrier
	s_waitcnt vmcnt(0)
	s_barrier
	s_mov_b64 s[0:1], exec
	v_readlane_b32 s2, v235, 5
	v_readlane_b32 s3, v235, 6
	s_and_b64 s[2:3], s[0:1], s[2:3]
	s_xor_b64 s[0:1], s[2:3], s[0:1]
	s_mov_b64 exec, s[2:3]
	s_cbranch_execz .LBB0_426
	s_cmp_eq_u32 s98, 0
	s_cbranch_scc1 .Lxb_nopend_3
	v_readlane_b32 s100, v235, 7
	v_readlane_b32 s101, v235, 8
	v_mov_b32_e32 v237, 0x3400
	s_nop 3

.Lxb_nopend_4:
	s_add_i32 s2, 0, 0x20000
	v_mov_b32_e32 v0, s2
	s_waitcnt vmcnt(0) expcnt(0) lgkmcnt(0)
	ds_read_b32 v2, v0
	s_add_i32 s2, 0, 0x20004
	v_mov_b32_e32 v0, s2
	ds_read_b32 v0, v0
	s_waitcnt lgkmcnt(1)
	v_cmp_ne_u32_e32 vcc, 0, v2
	s_cbranch_vccnz .LBB0_454
	v_readlane_b32 s44, v235, 0
	v_readlane_b32 s47, v235, 3
	v_readlane_b32 s2, v235, 4
	v_readlane_b32 s45, v235, 1
	s_mul_i32 s33, s47, s2
	s_add_u32 s2, s44, 0x1b6f200
	s_addc_u32 s3, s45, 0
	s_add_u32 s8, s44, 0x1b6f400
	s_addc_u32 s9, s45, 0
	s_add_u32 s10, s44, 0x1b6f500
	s_addc_u32 s11, s45, 0
	s_add_u32 s12, s44, 0x1b6f600
	s_addc_u32 s13, s45, 0
	s_add_u32 s14, s44, 0x1b6f700
	s_addc_u32 s15, s45, 0
	s_add_u32 s16, s44, 0x1b6f800
	s_addc_u32 s17, s45, 0
	s_add_u32 s18, s44, 0x1b6f900
	s_addc_u32 s19, s45, 0
	s_add_u32 s20, s44, 0x1b6fa00
	s_addc_u32 s21, s45, 0
	s_add_u32 s22, s44, 0x1b6fb00
	s_addc_u32 s23, s45, 0
	s_add_u32 s26, s44, 0x1b6fc00
	s_addc_u32 s27, s45, 0
	s_add_u32 s28, s44, 0x1b6fd00
	s_addc_u32 s29, s45, 0
	s_add_u32 s30, s44, 0x1b6fe00
	s_addc_u32 s31, s45, 0
	s_add_u32 s34, s44, 0x1b6ff00
	s_addc_u32 s35, s45, 0
	s_add_u32 s36, s44, 0x1b70000
	s_addc_u32 s37, s45, 0
	s_add_u32 s38, s44, 0x1b70100
	s_addc_u32 s39, s45, 0
	s_add_u32 s40, s44, 0x1b70200
	s_addc_u32 s41, s45, 0
	v_readlane_b32 s46, v235, 2
	s_add_u32 s42, s44, 0x1b70300
	s_mul_i32 s33, s33, s46
	s_addc_u32 s43, s45, 0
	s_mov_b32 s50, 1
	v_mov_b32_e32 v16, 0
	s_branch .LBB0_442

.LBB0_499:
	s_waitcnt vmcnt(0)
	s_waitcnt lgkmcnt(0)
	s_barrier
	s_mov_b64 s[0:1], exec
	v_readlane_b32 s2, v235, 5
	v_readlane_b32 s3, v235, 6
	s_and_b64 s[2:3], s[0:1], s[2:3]
	s_xor_b64 s[0:1], s[2:3], s[0:1]
	s_mov_b64 exec, s[2:3]
	s_cbranch_execz .LBB0_553
	s_cmp_eq_u32 s98, 0
	s_cbranch_scc1 .Lxb_nopend_5
	v_readlane_b32 s100, v235, 7
	v_readlane_b32 s101, v235, 8
	v_mov_b32_e32 v237, 0x3400
	s_nop 3

.Lxb_nopend_5:
	s_add_i32 s2, 0, 0x20000
	v_mov_b32_e32 v0, s2
	s_waitcnt vmcnt(0) expcnt(0) lgkmcnt(0)
	ds_read_b32 v2, v0
	s_add_i32 s2, 0, 0x20004
	v_mov_b32_e32 v0, s2
	ds_read_b32 v0, v0
	s_waitcnt lgkmcnt(1)
	v_cmp_ne_u32_e32 vcc, 0, v2
	s_cbranch_vccnz .LBB0_516
	v_readlane_b32 s40, v235, 0
	v_readlane_b32 s43, v235, 3
	v_readlane_b32 s2, v235, 4
	v_readlane_b32 s41, v235, 1
	s_mul_i32 s33, s43, s2
	s_add_u32 s2, s40, 0x1b6f200
	s_addc_u32 s3, s41, 0
	s_add_u32 s6, s40, 0x1b6f400
	s_addc_u32 s7, s41, 0
	s_add_u32 s8, s40, 0x1b6f500
	s_addc_u32 s9, s41, 0
	s_add_u32 s10, s40, 0x1b6f600
	s_addc_u32 s11, s41, 0
	s_add_u32 s12, s40, 0x1b6f700
	s_addc_u32 s13, s41, 0
	s_add_u32 s14, s40, 0x1b6f800
	s_addc_u32 s15, s41, 0
	s_add_u32 s16, s40, 0x1b6f900
	s_addc_u32 s17, s41, 0
	s_add_u32 s18, s40, 0x1b6fa00
	s_addc_u32 s19, s41, 0
	s_add_u32 s20, s40, 0x1b6fb00
	s_addc_u32 s21, s41, 0
	s_add_u32 s22, s40, 0x1b6fc00
	s_addc_u32 s23, s41, 0
	s_add_u32 s26, s40, 0x1b6fd00
	s_addc_u32 s27, s41, 0
	s_add_u32 s28, s40, 0x1b6fe00
	s_addc_u32 s29, s41, 0
	s_add_u32 s30, s40, 0x1b6ff00
	s_addc_u32 s31, s41, 0
	s_add_u32 s34, s40, 0x1b70000
	s_addc_u32 s35, s41, 0
	s_add_u32 s36, s40, 0x1b70100
	s_addc_u32 s37, s41, 0
	s_add_u32 s38, s40, 0x1b70200
	s_addc_u32 s39, s41, 0
	v_readlane_b32 s42, v235, 2
	s_add_u32 s40, s40, 0x1b70300
	s_mul_i32 s33, s33, s42
	s_addc_u32 s41, s41, 0
	s_mov_b32 s48, 1
	v_mov_b32_e32 v16, 0
	s_branch .LBB0_504

.LBB0_573:
	s_waitcnt vmcnt(0)
	s_barrier
	s_mov_b64 s[0:1], exec
	v_readlane_b32 s2, v235, 5
	v_readlane_b32 s3, v235, 6
	s_and_b64 s[2:3], s[0:1], s[2:3]
	s_xor_b64 s[0:1], s[2:3], s[0:1]
	s_mov_b64 exec, s[2:3]
	s_cbranch_execz .LBB0_626
	s_cmp_eq_u32 s98, 0
	s_cbranch_scc1 .Lxb_nopend_6
	v_readlane_b32 s100, v235, 7
	v_readlane_b32 s101, v235, 8
	v_mov_b32_e32 v237, 0x3400
	s_nop 3

.Lxb_nopend_6:
	s_add_i32 s2, 0, 0x20000
	v_mov_b32_e32 v0, s2
	s_waitcnt vmcnt(0) expcnt(0) lgkmcnt(0)
	ds_read_b32 v2, v0
	s_add_i32 s2, 0, 0x20004
	v_mov_b32_e32 v0, s2
	ds_read_b32 v0, v0
	s_waitcnt lgkmcnt(1)
	v_cmp_ne_u32_e32 vcc, 0, v2
	s_cbranch_vccnz .LBB0_589
	v_readlane_b32 s40, v235, 0
	v_readlane_b32 s43, v235, 3
	v_readlane_b32 s2, v235, 4
	v_readlane_b32 s41, v235, 1
	s_mul_i32 s33, s43, s2
	s_add_u32 s2, s40, 0x1b6f200
	s_addc_u32 s3, s41, 0
	s_add_u32 s4, s40, 0x1b6f400
	s_addc_u32 s5, s41, 0
	s_add_u32 s6, s40, 0x1b6f500
	s_addc_u32 s7, s41, 0
	s_add_u32 s8, s40, 0x1b6f600
	s_addc_u32 s9, s41, 0
	s_add_u32 s10, s40, 0x1b6f700
	s_addc_u32 s11, s41, 0
	s_add_u32 s12, s40, 0x1b6f800
	s_addc_u32 s13, s41, 0
	s_add_u32 s14, s40, 0x1b6f900
	s_addc_u32 s15, s41, 0
	s_add_u32 s16, s40, 0x1b6fa00
	s_addc_u32 s17, s41, 0
	s_add_u32 s18, s40, 0x1b6fb00
	s_addc_u32 s19, s41, 0
	s_add_u32 s20, s40, 0x1b6fc00
	s_addc_u32 s21, s41, 0
	s_add_u32 s22, s40, 0x1b6fd00
	s_addc_u32 s23, s41, 0
	s_add_u32 s26, s40, 0x1b6fe00
	s_addc_u32 s27, s41, 0
	s_add_u32 s28, s40, 0x1b6ff00
	s_addc_u32 s29, s41, 0
	s_add_u32 s30, s40, 0x1b70000
	s_addc_u32 s31, s41, 0
	s_add_u32 s34, s40, 0x1b70100
	s_addc_u32 s35, s41, 0
	s_add_u32 s36, s40, 0x1b70200
	s_addc_u32 s37, s41, 0
	v_readlane_b32 s42, v235, 2
	s_add_u32 s38, s40, 0x1b70300
	s_mul_i32 s33, s33, s42
	s_addc_u32 s39, s41, 0
	s_mov_b32 s46, 1
	v_mov_b32_e32 v16, 0
	s_branch .LBB0_577

.Lxb_nopend_7:
	s_add_i32 s2, 0, 0x20000
	v_mov_b32_e32 v0, s2
	s_waitcnt vmcnt(0) expcnt(0) lgkmcnt(0)
	ds_read_b32 v2, v0
	s_add_i32 s2, 0, 0x20004
	v_mov_b32_e32 v0, s2
	ds_read_b32 v0, v0
	s_waitcnt lgkmcnt(1)
	v_cmp_ne_u32_e32 vcc, 0, v2
	s_cbranch_vccnz .LBB0_675
	v_readlane_b32 s36, v235, 0
	v_readlane_b32 s39, v235, 3
	v_readlane_b32 s2, v235, 4
	v_readlane_b32 s37, v235, 1
	s_mul_i32 s33, s39, s2
	s_add_u32 s2, s36, 0x1b6f200
	s_addc_u32 s3, s37, 0
	s_add_u32 s4, s36, 0x1b6f400
	s_addc_u32 s5, s37, 0
	s_add_u32 s6, s36, 0x1b6f500
	s_addc_u32 s7, s37, 0
	s_add_u32 s8, s36, 0x1b6f600
	s_addc_u32 s9, s37, 0
	s_add_u32 s10, s36, 0x1b6f700
	s_addc_u32 s11, s37, 0
	s_add_u32 s12, s36, 0x1b6f800
	s_addc_u32 s13, s37, 0
	s_add_u32 s14, s36, 0x1b6f900
	s_addc_u32 s15, s37, 0
	s_add_u32 s16, s36, 0x1b6fa00
	s_addc_u32 s17, s37, 0
	s_add_u32 s18, s36, 0x1b6fb00
	s_addc_u32 s19, s37, 0
	s_add_u32 s20, s36, 0x1b6fc00
	s_addc_u32 s21, s37, 0
	s_add_u32 s22, s36, 0x1b6fd00
	s_addc_u32 s23, s37, 0
	s_add_u32 s24, s36, 0x1b6fe00
	s_addc_u32 s25, s37, 0
	s_add_u32 s26, s36, 0x1b6ff00
	s_addc_u32 s27, s37, 0
	s_add_u32 s28, s36, 0x1b70000
	s_addc_u32 s29, s37, 0
	s_add_u32 s30, s36, 0x1b70100
	s_addc_u32 s31, s37, 0
	s_add_u32 s34, s36, 0x1b70200
	s_addc_u32 s35, s37, 0
	v_readlane_b32 s38, v235, 2
	s_add_u32 s36, s36, 0x1b70300
	s_mul_i32 s33, s33, s38
	s_addc_u32 s37, s37, 0
	s_mov_b32 s44, 1
	v_mov_b32_e32 v16, 0
	s_branch .LBB0_663

.Lxb_poll_7:
	v_readlane_b32 s101, v235, 2
	v_readlane_b32 s100, v235, 16
	s_cmp_lt_u32 s101, 64
	s_cbranch_scc1 .Lxb_wait_7
	s_cmp_ge_u32 s100, 32
	s_cbranch_scc0 .Lxb_wait_7
	v_readfirstlane_b32 s98, v236
	s_branch .Lxb_done_7

.LBB0_919:
	s_waitcnt vmcnt(0)
	s_waitcnt vmcnt(63) expcnt(7) lgkmcnt(15)
	s_barrier
	s_mov_b64 s[0:1], exec
	v_readlane_b32 s2, v235, 5
	v_readlane_b32 s3, v235, 6
	s_and_b64 s[2:3], s[0:1], s[2:3]
	s_xor_b64 s[0:1], s[2:3], s[0:1]
	s_mov_b64 exec, s[2:3]
	s_cbranch_execz .LBB0_972
	s_cmp_eq_u32 s98, 0
	s_cbranch_scc1 .Lxb_nopend_8
	v_readlane_b32 s100, v235, 7
	v_readlane_b32 s101, v235, 8
	v_mov_b32_e32 v237, 0x3400
	s_nop 3

.LBB0_976:
	s_or_b64 exec, exec, s[2:3]
	s_waitcnt vmcnt(0)
	s_barrier
	s_mov_b64 s[2:3], exec
	v_readlane_b32 s4, v235, 5
	v_readlane_b32 s5, v235, 6
	s_and_b64 s[4:5], s[2:3], s[4:5]
	s_xor_b64 s[2:3], s[4:5], s[2:3]
	s_mov_b64 exec, s[4:5]
	s_cbranch_execz .LBB0_1029
	s_cmp_eq_u32 s98, 0
	s_cbranch_scc1 .Lxb_nopend_9
	v_readlane_b32 s100, v235, 7
	v_readlane_b32 s101, v235, 8
	v_mov_b32_e32 v237, 0x3400
	s_nop 3

.Lxb_nopend_9:
	s_add_i32 s4, 0, 0x20000
	v_mov_b32_e32 v0, s4
	s_waitcnt vmcnt(0) expcnt(0) lgkmcnt(0)
	ds_read_b32 v2, v0
	s_add_i32 s4, 0, 0x20004
	v_mov_b32_e32 v0, s4
	ds_read_b32 v0, v0
	s_waitcnt lgkmcnt(1)
	v_cmp_ne_u32_e32 vcc, 0, v2
	s_cbranch_vccnz .LBB0_992
	v_readlane_b32 s40, v235, 0
	v_readlane_b32 s43, v235, 3
	v_readlane_b32 s4, v235, 4
	v_readlane_b32 s41, v235, 1
	s_mul_i32 s33, s43, s4
	s_add_u32 s4, s40, 0x1b6f200
	s_addc_u32 s5, s41, 0
	s_add_u32 s6, s40, 0x1b6f400
	s_addc_u32 s7, s41, 0
	s_add_u32 s8, s40, 0x1b6f500
	s_addc_u32 s9, s41, 0
	s_add_u32 s10, s40, 0x1b6f600
	s_addc_u32 s11, s41, 0
	s_add_u32 s12, s40, 0x1b6f700
	s_addc_u32 s13, s41, 0
	s_add_u32 s14, s40, 0x1b6f800
	s_addc_u32 s15, s41, 0
	s_add_u32 s16, s40, 0x1b6f900
	s_addc_u32 s17, s41, 0
	s_add_u32 s18, s40, 0x1b6fa00
	s_addc_u32 s19, s41, 0
	s_add_u32 s20, s40, 0x1b6fb00
	s_addc_u32 s21, s41, 0
	s_add_u32 s22, s40, 0x1b6fc00
	s_addc_u32 s23, s41, 0
	s_add_u32 s24, s40, 0x1b6fd00
	s_addc_u32 s25, s41, 0
	s_add_u32 s26, s40, 0x1b6fe00
	s_addc_u32 s27, s41, 0
	s_add_u32 s28, s40, 0x1b6ff00
	s_addc_u32 s29, s41, 0
	s_add_u32 s30, s40, 0x1b70000
	s_addc_u32 s31, s41, 0
	s_add_u32 s34, s40, 0x1b70100
	s_addc_u32 s35, s41, 0
	s_add_u32 s36, s40, 0x1b70200
	s_addc_u32 s37, s41, 0
	v_readlane_b32 s42, v235, 2
	s_add_u32 s38, s40, 0x1b70300
	s_mul_i32 s33, s33, s42
	s_addc_u32 s39, s41, 0
	s_mov_b32 s46, 1
	v_mov_b32_e32 v16, 0
	s_branch .LBB0_980

.LBB0_1115:
	s_waitcnt vmcnt(0)
	s_waitcnt vmcnt(0) lgkmcnt(0)
	s_barrier
	s_mov_b64 s[0:1], exec
	v_readlane_b32 s2, v235, 5
	v_readlane_b32 s3, v235, 6
	s_and_b64 s[2:3], s[0:1], s[2:3]
	s_xor_b64 s[0:1], s[2:3], s[0:1]
	s_mov_b64 exec, s[2:3]
	s_cbranch_execz .LBB0_1168
	s_cmp_eq_u32 s98, 0
	s_cbranch_scc1 .Lxb_nopend_10
	v_readlane_b32 s100, v235, 7
	v_readlane_b32 s101, v235, 8
	v_mov_b32_e32 v237, 0x3400
	s_nop 3

.Lxb_nopend_10:
	s_add_i32 s2, 0, 0x20000
	v_mov_b32_e32 v0, s2
	s_waitcnt vmcnt(0) expcnt(0) lgkmcnt(0)
	ds_read_b32 v2, v0
	s_add_i32 s2, 0, 0x20004
	v_mov_b32_e32 v0, s2
	ds_read_b32 v0, v0
	s_waitcnt lgkmcnt(1)
	v_cmp_ne_u32_e32 vcc, 0, v2
	s_cbranch_vccnz .LBB0_1131
	v_readlane_b32 s40, v235, 0
	v_readlane_b32 s43, v235, 3
	v_readlane_b32 s2, v235, 4
	v_readlane_b32 s41, v235, 1
	s_mul_i32 s23, s43, s2
	s_add_u32 s2, s40, 0x1b6f200
	s_addc_u32 s3, s41, 0
	s_add_u32 s4, s40, 0x1b6f400
	s_addc_u32 s5, s41, 0
	s_add_u32 s6, s40, 0x1b6f500
	s_addc_u32 s7, s41, 0
	s_add_u32 s8, s40, 0x1b6f600
	s_addc_u32 s9, s41, 0
	s_add_u32 s10, s40, 0x1b6f700
	s_addc_u32 s11, s41, 0
	s_add_u32 s12, s40, 0x1b6f800
	s_addc_u32 s13, s41, 0
	s_add_u32 s14, s40, 0x1b6f900
	s_addc_u32 s15, s41, 0
	s_add_u32 s16, s40, 0x1b6fa00
	s_addc_u32 s17, s41, 0
	s_add_u32 s18, s40, 0x1b6fb00
	s_addc_u32 s19, s41, 0
	s_add_u32 s20, s40, 0x1b6fc00
	s_addc_u32 s21, s41, 0
	s_add_u32 s24, s40, 0x1b6fd00
	s_addc_u32 s25, s41, 0
	s_add_u32 s26, s40, 0x1b6fe00
	s_addc_u32 s27, s41, 0
	s_add_u32 s28, s40, 0x1b6ff00
	s_addc_u32 s29, s41, 0
	s_add_u32 s30, s40, 0x1b70000
	s_addc_u32 s31, s41, 0
	s_add_u32 s34, s40, 0x1b70100
	s_addc_u32 s35, s41, 0
	s_add_u32 s36, s40, 0x1b70200
	s_addc_u32 s37, s41, 0
	v_readlane_b32 s42, v235, 2
	s_add_u32 s38, s40, 0x1b70300
	s_mul_i32 s23, s23, s42
	s_addc_u32 s39, s41, 0
	s_mov_b32 s33, 1
	v_mov_b32_e32 v16, 0
	s_branch .LBB0_1119

.LBB0_1188:
	s_waitcnt vmcnt(0)
	s_barrier
	s_mov_b64 s[0:1], exec
	v_readlane_b32 s2, v235, 5
	v_readlane_b32 s3, v235, 6
	s_and_b64 s[2:3], s[0:1], s[2:3]
	v_readlane_b32 s46, v235, 14
	s_xor_b64 s[0:1], s[2:3], s[0:1]
	v_readlane_b32 s47, v235, 15
	s_mov_b64 exec, s[2:3]
	s_cbranch_execz .LBB0_1241
	s_cmp_eq_u32 s98, 0
	s_cbranch_scc1 .Lxb_nopend_11
	v_readlane_b32 s100, v235, 7
	v_readlane_b32 s101, v235, 8
	v_mov_b32_e32 v237, 0x3400
	s_nop 3
